# expert-down: the per-piece LDS drain moved out of the loop (one wait in the peeled first piece covers the first iteration; later iterations are covered by the destination-row wait of the previous piec
# baseline (speedup 1.0000x reference)
; #define D2_READA(par, it_) do { const unsigned _zb = (unsigned)((it_) & (NS - 1)) * PB; _Pragma("unroll") for (int _k = 0; _k < 2; ++_k) _Pragma("unroll") for (int _m = 0; _m < 2; ++_m) \
;         Af[par][_k][_m].w = cat8(*(const LAS bf16x8*)(lds + _zb + _k * 8192 + aoff + _m * 2048), *(const LAS bf16x8*)(lds + _zb + _k * 8192 + aoff + _m * 2048 + 1024)); } while (0)
;     ...
;     D2_READA(0, 0);
;     D2_PIECE(0, 0, false);
.LBB0_751:
	v_mov_b32_e32 v0, s4
	ds_read_b32 v207, v0
	s_add_i32 s18, s18, 1
	s_add_i32 s4, s4, 4
	s_waitcnt lgkmcnt(0)
	v_cmp_ge_i32_e32 vcc, s10, v207
	s_cbranch_vccnz .LBB0_751
	s_add_u32 s4, s16, 0x2000000
	s_addc_u32 s5, s17, 0
	s_add_u32 s16, s16, 0xa000000
	v_readlane_b32 s7, v252, 12
	s_addc_u32 s17, s17, 0
	s_ashr_i32 s19, s18, 31
	s_lshl_b32 s7, s7, 8
	s_lshl_b64 s[22:23], s[18:19], 10
	s_and_b32 s20, s7, 0x300
	s_or_b32 s7, s22, s20
	s_and_b32 s22, s21, 0xc0
	v_lshlrev_b32_e32 v0, 2, v202
	s_or_b32 s7, s7, s22
	v_and_b32_e32 v162, 48, v0
	v_and_b32_e32 v163, 3, v12
	v_or3_b32 v0, s7, v162, v163
	v_mov_b32_e32 v1, s23
	v_lshlrev_b64 v[0:1], 8, v[0:1]
	v_mov_b32_e32 v161, 0
	v_lshl_add_u64 v[0:1], s[4:5], 0, v[0:1]
	v_lshl_add_u64 v[60:61], v[0:1], 0, v[160:161]
	global_load_dwordx4 v[0:3], v[60:61], off
	global_load_dwordx4 v[4:7], v[60:61], off offset:64
	global_load_dwordx4 v[8:11], v[60:61], off offset:1024
	global_load_dwordx4 v[12:15], v[60:61], off offset:1088
	global_load_dwordx4 v[16:19], v[60:61], off offset:2048
	global_load_dwordx4 v[20:23], v[60:61], off offset:2112
	global_load_dwordx4 v[24:27], v[60:61], off offset:3072
	global_load_dwordx4 v[28:31], v[60:61], off offset:3136
	global_load_dwordx4 v[32:35], v[60:61], off offset:128
	global_load_dwordx4 v[36:39], v[60:61], off offset:192
	global_load_dwordx4 v[40:43], v[60:61], off offset:1152
	global_load_dwordx4 v[44:47], v[60:61], off offset:1216
	global_load_dwordx4 v[48:51], v[60:61], off offset:2176
	global_load_dwordx4 v[52:55], v[60:61], off offset:2240
	global_load_dwordx4 v[56:59], v[60:61], off offset:3200
	s_nop 0
	global_load_dwordx4 v[60:63], v[60:61], off offset:3264
	s_mov_b32 s21, 0
	s_mov_b32 s23, s21
	s_sub_i32 s25, s6, s10
	s_waitcnt vmcnt(0)
	ds_read_b128 v[64:67], v206 offset:16384
	ds_read_b128 v[68:71], v206 offset:17408
	ds_read_b128 v[72:75], v206 offset:18432
	ds_read_b128 v[76:79], v206 offset:19456
	ds_read_b128 v[80:83], v206 offset:24576
	ds_read_b128 v[84:87], v206 offset:25600
	ds_read_b128 v[88:91], v206 offset:26624
	ds_read_b128 v[92:95], v206 offset:27648
	v_mfma_f32_16x16x128_f8f6f4 v[132:135], v[0:7], v[120:127], 0
	v_mfma_f32_16x16x128_f8f6f4 v[128:131], v[8:15], v[120:127], 0
	v_mfma_f32_16x16x128_f8f6f4 v[140:143], v[16:23], v[120:127], 0
	v_mfma_f32_16x16x128_f8f6f4 v[136:139], v[24:31], v[120:127], 0
	v_mfma_f32_16x16x128_f8f6f4 v[148:151], v[0:7], v[112:119], 0
	v_mfma_f32_16x16x128_f8f6f4 v[144:147], v[8:15], v[112:119], 0
	v_mfma_f32_16x16x128_f8f6f4 v[156:159], v[16:23], v[112:119], 0
	v_mfma_f32_16x16x128_f8f6f4 v[152:155], v[24:31], v[112:119], 0
	s_waitcnt lgkmcnt(0)
	v_mfma_f32_16x16x128_f8f6f4 v[132:135], v[32:39], v[104:111], v[132:135]
	v_mfma_f32_16x16x128_f8f6f4 v[128:131], v[40:47], v[104:111], v[128:131]
	v_mfma_f32_16x16x128_f8f6f4 v[140:143], v[48:55], v[104:111], v[140:143]
	v_mfma_f32_16x16x128_f8f6f4 v[136:139], v[56:63], v[104:111], v[136:139]
	v_mfma_f32_16x16x128_f8f6f4 v[148:151], v[32:39], v[96:103], v[148:151]
	v_mfma_f32_16x16x128_f8f6f4 v[144:147], v[40:47], v[96:103], v[144:147]
	v_mfma_f32_16x16x128_f8f6f4 v[156:159], v[48:55], v[96:103], v[156:159]
	v_mfma_f32_16x16x128_f8f6f4 v[152:155], v[56:63], v[96:103], v[152:155]
	s_cmp_gt_i32 s25, 1
	v_or_b32_e32 v96, s22, v160
	s_cbranch_scc1 .LBB0_771
	v_or_b32_e32 v192, s20, v96
	v_mov_b32_e32 v193, v161
	s_cbranch_execz .LBB0_772
